# baseline (speedup 1.0000x reference)
.LBB2_4:
	s_or_b64 exec, exec, s[4:5]
	v_mov_b32_e32 v17, 0
	s_waitcnt lgkmcnt(0)
	s_barrier
	ds_read_b32 v2, v17 offset:32776
	s_load_dwordx4 s[4:7], s[0:1], 0x8
	v_lshrrev_b32_e32 v1, 6, v0
	v_and_b32_e32 v28, 63, v0
	s_movk_i32 s3, 0x1000
	s_waitcnt lgkmcnt(0)
	v_readfirstlane_b32 s0, v2
	s_and_b32 s24, s0, 31
	v_lshlrev_b32_e32 v2, 16, v1
	v_lshl_or_b32 v2, s24, 18, v2
	v_lshl_or_b32 v16, v28, 5, v2
	v_lshl_add_u64 v[2:3], s[14:15], 0, v[16:17]
	v_mov_b32_e32 v115, 0
	v_lshlrev_b32_e32 v110, 11, v1
	v_add_u32_e32 v111, 1, v1
	v_and_b32_e32 v111, 3, v111
	v_lshlrev_b32_e32 v111, 11, v111
	v_add_u32_e32 v112, 2, v1
	v_and_b32_e32 v112, 3, v112
	v_lshlrev_b32_e32 v112, 11, v112
	v_add_u32_e32 v113, 3, v1
	v_and_b32_e32 v113, 3, v113
	v_lshlrev_b32_e32 v113, 11, v113
	v_mov_b32_e32 v114, v110
	v_lshl_add_u64 v[116:117], v[2:3], 0, v[114:115]
	global_load_dwordx4 a[0:3], v[116:117], off
	global_load_dwordx4 a[4:7], v[116:117], off offset:16
	v_add_u32_e32 v114, 0x2000, v110
	v_lshl_add_u64 v[116:117], v[2:3], 0, v[114:115]
	global_load_dwordx4 a[8:11], v[116:117], off
	global_load_dwordx4 a[12:15], v[116:117], off offset:16
	v_add_u32_e32 v114, 0x4000, v110
	v_lshl_add_u64 v[116:117], v[2:3], 0, v[114:115]
	global_load_dwordx4 a[16:19], v[116:117], off
	global_load_dwordx4 a[20:23], v[116:117], off offset:16
	v_add_u32_e32 v114, 0x6000, v110
	v_lshl_add_u64 v[116:117], v[2:3], 0, v[114:115]
	global_load_dwordx4 a[24:27], v[116:117], off
	global_load_dwordx4 a[28:31], v[116:117], off offset:16
	v_mov_b32_e32 v114, v111
	v_lshl_add_u64 v[116:117], v[2:3], 0, v[114:115]
	global_load_dwordx4 a[32:35], v[116:117], off
	global_load_dwordx4 a[36:39], v[116:117], off offset:16
	v_add_u32_e32 v114, 0x2000, v111
	v_lshl_add_u64 v[116:117], v[2:3], 0, v[114:115]
	global_load_dwordx4 a[40:43], v[116:117], off
	global_load_dwordx4 a[44:47], v[116:117], off offset:16
	v_add_u32_e32 v114, 0x4000, v111
	v_lshl_add_u64 v[116:117], v[2:3], 0, v[114:115]
	global_load_dwordx4 a[48:51], v[116:117], off
	global_load_dwordx4 a[52:55], v[116:117], off offset:16
	v_add_u32_e32 v114, 0x6000, v111
	v_lshl_add_u64 v[116:117], v[2:3], 0, v[114:115]
	global_load_dwordx4 a[56:59], v[116:117], off
	global_load_dwordx4 a[60:63], v[116:117], off offset:16
	v_mov_b32_e32 v114, v112
	v_lshl_add_u64 v[116:117], v[2:3], 0, v[114:115]
	global_load_dwordx4 a[64:67], v[116:117], off
	global_load_dwordx4 a[68:71], v[116:117], off offset:16
	v_add_u32_e32 v114, 0x2000, v112
	v_lshl_add_u64 v[116:117], v[2:3], 0, v[114:115]
	global_load_dwordx4 a[72:75], v[116:117], off
	global_load_dwordx4 a[76:79], v[116:117], off offset:16
	v_add_u32_e32 v114, 0x4000, v112
	v_lshl_add_u64 v[116:117], v[2:3], 0, v[114:115]
	global_load_dwordx4 a[80:83], v[116:117], off
	global_load_dwordx4 a[84:87], v[116:117], off offset:16
	v_add_u32_e32 v114, 0x6000, v112
	v_lshl_add_u64 v[116:117], v[2:3], 0, v[114:115]
	global_load_dwordx4 a[88:91], v[116:117], off
	global_load_dwordx4 a[92:95], v[116:117], off offset:16
	v_mov_b32_e32 v114, v113
	v_lshl_add_u64 v[116:117], v[2:3], 0, v[114:115]
	global_load_dwordx4 a[96:99], v[116:117], off
	global_load_dwordx4 a[100:103], v[116:117], off offset:16
	v_add_u32_e32 v114, 0x2000, v113
	v_lshl_add_u64 v[116:117], v[2:3], 0, v[114:115]
	global_load_dwordx4 a[104:107], v[116:117], off
	global_load_dwordx4 a[108:111], v[116:117], off offset:16
	v_add_u32_e32 v114, 0x4000, v113
	v_lshl_add_u64 v[116:117], v[2:3], 0, v[114:115]
	global_load_dwordx4 a[112:115], v[116:117], off
	global_load_dwordx4 a[116:119], v[116:117], off offset:16
	v_add_u32_e32 v114, 0x6000, v113
	v_lshl_add_u64 v[116:117], v[2:3], 0, v[114:115]
	global_load_dwordx4 a[120:123], v[116:117], off
	global_load_dwordx4 a[124:127], v[116:117], off offset:16
	v_add_u32_e32 v114, 0x8000, v110
	v_lshl_add_u64 v[116:117], v[2:3], 0, v[114:115]
	global_load_dwordx4 a[128:131], v[116:117], off
	global_load_dwordx4 a[132:135], v[116:117], off offset:16
	v_add_u32_e32 v114, 0xa000, v110
	v_lshl_add_u64 v[116:117], v[2:3], 0, v[114:115]
	global_load_dwordx4 a[136:139], v[116:117], off
	global_load_dwordx4 a[140:143], v[116:117], off offset:16
	v_add_u32_e32 v114, 0xc000, v110
	v_lshl_add_u64 v[116:117], v[2:3], 0, v[114:115]
	global_load_dwordx4 a[144:147], v[116:117], off
	global_load_dwordx4 a[148:151], v[116:117], off offset:16
	v_add_u32_e32 v114, 0xe000, v110
	v_lshl_add_u64 v[116:117], v[2:3], 0, v[114:115]
	global_load_dwordx4 a[152:155], v[116:117], off
	global_load_dwordx4 a[156:159], v[116:117], off offset:16
	v_add_u32_e32 v114, 0x8000, v111
	v_lshl_add_u64 v[116:117], v[2:3], 0, v[114:115]
	global_load_dwordx4 a[160:163], v[116:117], off
	global_load_dwordx4 a[164:167], v[116:117], off offset:16
	v_add_u32_e32 v114, 0xa000, v111
	v_lshl_add_u64 v[116:117], v[2:3], 0, v[114:115]
	global_load_dwordx4 a[168:171], v[116:117], off
	global_load_dwordx4 a[172:175], v[116:117], off offset:16
	v_add_u32_e32 v114, 0xc000, v111
	v_lshl_add_u64 v[116:117], v[2:3], 0, v[114:115]
	global_load_dwordx4 a[176:179], v[116:117], off
	global_load_dwordx4 a[180:183], v[116:117], off offset:16
	v_add_u32_e32 v114, 0xe000, v111
	v_lshl_add_u64 v[116:117], v[2:3], 0, v[114:115]
	global_load_dwordx4 a[184:187], v[116:117], off
	global_load_dwordx4 a[188:191], v[116:117], off offset:16
	v_add_u32_e32 v114, 0x8000, v112
	v_lshl_add_u64 v[116:117], v[2:3], 0, v[114:115]
	global_load_dwordx4 a[192:195], v[116:117], off
	global_load_dwordx4 a[196:199], v[116:117], off offset:16
	v_add_u32_e32 v114, 0xa000, v112
	v_lshl_add_u64 v[116:117], v[2:3], 0, v[114:115]
	global_load_dwordx4 a[200:203], v[116:117], off
	global_load_dwordx4 a[204:207], v[116:117], off offset:16
	v_add_u32_e32 v114, 0xc000, v112
	v_lshl_add_u64 v[116:117], v[2:3], 0, v[114:115]
	global_load_dwordx4 a[208:211], v[116:117], off
	global_load_dwordx4 a[212:215], v[116:117], off offset:16
	v_add_u32_e32 v114, 0xe000, v112
	v_lshl_add_u64 v[116:117], v[2:3], 0, v[114:115]
	global_load_dwordx4 a[216:219], v[116:117], off
	global_load_dwordx4 a[220:223], v[116:117], off offset:16
	v_add_u32_e32 v114, 0x8000, v113
	v_lshl_add_u64 v[116:117], v[2:3], 0, v[114:115]
	global_load_dwordx4 a[224:227], v[116:117], off
	global_load_dwordx4 a[228:231], v[116:117], off offset:16
	v_add_u32_e32 v114, 0xa000, v113
	v_lshl_add_u64 v[116:117], v[2:3], 0, v[114:115]
	global_load_dwordx4 a[232:235], v[116:117], off
	global_load_dwordx4 a[236:239], v[116:117], off offset:16
	v_add_u32_e32 v114, 0xc000, v113
	v_lshl_add_u64 v[116:117], v[2:3], 0, v[114:115]
	global_load_dwordx4 a[240:243], v[116:117], off
	global_load_dwordx4 a[244:247], v[116:117], off offset:16
	v_add_u32_e32 v114, 0xe000, v113
	v_lshl_add_u64 v[116:117], v[2:3], 0, v[114:115]
	global_load_dwordx4 a[248:251], v[116:117], off
	global_load_dwordx4 a[252:255], v[116:117], off offset:16
	s_movk_i32 s12, 0x2000
	s_movk_i32 s13, 0x3000
	v_lshlrev_b32_e32 v29, 3, v1
	s_lshl_b32 s18, s24, 5
	s_cmp_lt_u32 s24, 16
	s_cselect_b64 s[22:23], -1, 0
	s_and_b64 s[16:17], s[22:23], exec
	s_movk_i32 s0, 0x800
	s_cselect_b32 s0, s0, 0x1800
	s_mov_b32 s1, 0
	v_bfe_u32 v4, v0, 3, 1
	v_and_b32_e32 v5, 7, v0
	v_or3_b32 v16, s18, v29, v5
	v_lshlrev_b32_e32 v7, 1, v4
	v_lshrrev_b32_e32 v3, 2, v0
	v_bfe_u32 v2, v0, 5, 1
	v_and_b32_e32 v6, 4, v3
	v_or3_b32 v6, v6, v7, v2
	v_mov_b32_e32 v3, v17
	v_lshlrev_b32_e32 v2, 1, v16
	ds_read_b32 v27, v17 offset:32772
	s_waitcnt lgkmcnt(0)
	v_lshl_or_b32 v18, v27, 3, v6
	v_ashrrev_i32_e32 v19, 31, v18
	v_lshlrev_b64 v[8:9], 20, v[18:19]
	v_lshl_add_u64 v[10:11], s[4:5], 0, v[8:9]
	v_lshl_add_u64 v[20:21], v[10:11], 0, v[2:3]
	v_add_co_u32_e32 v24, vcc, s3, v20
	v_lshl_add_u64 v[8:9], s[6:7], 0, v[8:9]
	s_nop 0
	v_addc_co_u32_e32 v25, vcc, 0, v21, vcc
	v_add_co_u32_e32 v12, vcc, s12, v20
	v_lshl_add_u64 v[2:3], v[8:9], 0, v[2:3]
	s_nop 0
	v_addc_co_u32_e32 v13, vcc, 0, v21, vcc
	v_add_co_u32_e32 v30, vcc, s13, v20
	v_lshl_add_u64 v[22:23], v[2:3], 0, s[0:1]
	s_nop 0
	v_addc_co_u32_e32 v31, vcc, 0, v21, vcc
	v_add_co_u32_e32 v2, vcc, 0x2000, v22
	global_load_ushort v8, v[20:21], off
	global_load_ushort v9, v[20:21], off offset:2048
	global_load_ushort v11, v[12:13], off offset:-4096
	global_load_ushort v10, v[12:13], off
	s_nop 0
	global_load_ushort v12, v[12:13], off offset:2048
	v_addc_co_u32_e32 v3, vcc, 0, v23, vcc
	global_load_ushort v14, v[22:23], off
	s_nop 0
	global_load_ushort v24, v[24:25], off offset:2048
	s_nop 0
	global_load_ushort v13, v[30:31], off
	global_load_ushort v15, v[30:31], off offset:2048
	global_load_ushort v25, v[2:3], off
	s_waitcnt vmcnt(0)
	v_cmp_gt_u32_e32 vcc, 64, v0
	s_and_saveexec_b64 s[12:13], vcc
	s_cbranch_execz .LBB2_9
	v_lshlrev_b32_e32 v2, 2, v5
	v_mov_b32_e32 v3, v17
	v_lshl_add_u64 v[2:3], s[10:11], 0, v[2:3]
